# on top of the MoE expert-table hoist: P9 K-loop header takes one compare+branch for iterations before the last two; the two s_nop 15 at the P9/P10 epilogue start removed (>=12 independent instructions
# speedup vs baseline: 1.0223x; 1.0068x over previous
.LBB0_1356:
	s_add_u32 s50, s44, 0x80
	s_addc_u32 s51, s45, 0
	s_add_u32 s37, s44, 0x100
	s_addc_u32 s49, s45, 0
	s_add_u32 s52, s38, 0x100
	s_addc_u32 s53, s39, 0
	s_cmp_eq_u32 s29, 12
	s_cselect_b64 s[6:7], -1, 0
	s_and_b64 s[46:47], s[6:7], exec
	s_cselect_b32 s48, s40, s37
	s_cselect_b32 s49, s41, s49
	s_cselect_b32 s46, s30, s52
	s_cselect_b32 s47, s31, s53
	s_cmp_lt_i32 s29, 10
	s_cbranch_scc1 .LBB0_1355
	s_cmp_lg_u32 s29, 12
	s_cbranch_scc1 .Lp9_nofin
	s_andn2_b64 vcc, exec, s[4:5]
	s_cbranch_vccnz .Lp9_nofin
	v_lshl_add_u32 v192, v230, 11, v183
	v_lshl_add_u32 v191, v231, 11, v184
	v_lshl_add_u32 v190, v232, 11, v183
	v_lshl_add_u32 v193, v233, 11, v184

.LBB0_1370:
	s_ashr_i32 s37, s36, 31
	s_lshl_b64 s[6:7], s[36:37], 14
	v_lshl_or_b32 v22, s34, 7, v186
	s_add_u32 s6, s10, s6
	s_addc_u32 s7, s11, s7
	v_ashrrev_i32_e32 v23, 31, v22
	s_mov_b64 s[6:7], 0x2000
	v_lshl_add_u32 v18, v195, 8, v171
	v_or_b32_e32 v24, 16, v18
	v_or_b32_e32 v26, 32, v18
	v_or_b32_e32 v28, 48, v18
	v_ashrrev_i32_e32 v19, 31, v18
	v_ashrrev_i32_e32 v25, 31, v24
	v_ashrrev_i32_e32 v27, 31, v26
	v_ashrrev_i32_e32 v29, 31, v28
	v_lshlrev_b64 v[18:19], 11, v[18:19]
	v_lshlrev_b64 v[24:25], 11, v[24:25]
	v_lshlrev_b64 v[26:27], 11, v[26:27]
	v_lshlrev_b64 v[28:29], 11, v[28:29]
	v_lshl_add_u64 v[18:19], s[14:15], 0, v[18:19]
	v_lshl_add_u64 v[24:25], s[14:15], 0, v[24:25]
	v_lshl_add_u64 v[26:27], s[14:15], 0, v[26:27]
	v_lshl_add_u64 v[28:29], s[14:15], 0, v[28:29]
	v_lshl_add_u64 v[18:19], v[18:19], 0, v[22:23]
	v_lshl_add_u64 v[24:25], v[24:25], 0, v[22:23]
	v_lshl_add_u64 v[26:27], v[26:27], 0, v[22:23]
	v_lshl_add_u64 v[22:23], v[28:29], 0, v[22:23]
	v_mov_b32_e32 v20, v163
	v_mov_b32_e32 v21, v163
	s_mov_b32 s6, 0x40000
	v_mov_b64_e32 v[6:7], v[234:235]
	v_mov_b64_e32 v[8:9], v[236:237]
	v_mov_b64_e32 v[14:15], v[238:239]
	v_mov_b64_e32 v[16:17], v[240:241]
	v_mov_b64_e32 v[10:11], v[242:243]
	v_mov_b64_e32 v[12:13], v[244:245]
	v_mov_b64_e32 v[2:3], v[246:247]
	v_mov_b64_e32 v[4:5], v[248:249]
	v_pk_fma_f32 v[32:33], v[154:155], s[22:23], v[6:7] op_sel_hi:[1,0,1]
	v_pk_fma_f32 v[28:29], v[158:159], s[22:23], v[14:15] op_sel_hi:[1,0,1]
	v_pk_fma_f32 v[154:155], v[156:157], s[22:23], v[8:9] op_sel_hi:[1,0,1]
	v_min_f32_e32 v28, 0x40e00000, v28
	v_min_f32_e32 v29, 0x40e00000, v29
	v_min_f32_e32 v32, 0x40e00000, v32
	v_min_f32_e32 v33, 0x40e00000, v33
	v_pk_mul_f32 v[156:157], v[28:29], s[24:25] op_sel_hi:[1,0]
	v_pk_fma_f32 v[30:31], v[160:161], s[22:23], v[16:17] op_sel_hi:[1,0,1]
	v_pk_mul_f32 v[160:161], v[32:33], s[24:25] op_sel_hi:[1,0]
	v_exp_f32_e32 v156, v156
	v_exp_f32_e32 v157, v157
	v_exp_f32_e32 v160, v160
	v_exp_f32_e32 v161, v161
	v_min_f32_e32 v30, 0x40e00000, v30
	v_min_f32_e32 v31, 0x40e00000, v31
	v_min_f32_e32 v154, 0x40e00000, v154
	v_min_f32_e32 v155, 0x40e00000, v155
	v_pk_mul_f32 v[158:159], v[30:31], s[24:25] op_sel_hi:[1,0]
	v_pk_mul_f32 v[168:169], v[154:155], s[24:25] op_sel_hi:[1,0]
	v_exp_f32_e32 v158, v158
	v_exp_f32_e32 v159, v159
	v_pk_add_f32 v[156:157], v[156:157], 1.0 op_sel_hi:[1,0]
	v_exp_f32_e32 v168, v168
	v_exp_f32_e32 v169, v169
	v_pk_add_f32 v[160:161], v[160:161], 1.0 op_sel_hi:[1,0]
	v_rcp_f32_e32 v156, v156
	v_rcp_f32_e32 v157, v157
	v_rcp_f32_e32 v160, v160
	v_rcp_f32_e32 v161, v161
	v_pk_fma_f32 v[150:151], v[150:151], s[22:23], v[10:11] op_sel_hi:[1,0,1]
	v_pk_fma_f32 v[146:147], v[146:147], s[22:23], v[2:3] op_sel_hi:[1,0,1]
	v_med3_f32 v150, v150, s87, v189
	v_med3_f32 v151, v151, s87, v189
	v_pk_add_f32 v[158:159], v[158:159], 1.0 op_sel_hi:[1,0]
	v_med3_f32 v146, v146, s87, v189
	v_med3_f32 v147, v147, s87, v189
	v_pk_add_f32 v[150:151], v[150:151], 1.0 op_sel_hi:[1,0]
	v_pk_add_f32 v[168:169], v[168:169], 1.0 op_sel_hi:[1,0]
	v_rcp_f32_e32 v158, v158
	v_rcp_f32_e32 v159, v159
	v_pk_mul_f32 v[28:29], v[28:29], v[156:157]
	v_pk_add_f32 v[146:147], v[146:147], 1.0 op_sel_hi:[1,0]
	v_rcp_f32_e32 v168, v168
	v_rcp_f32_e32 v169, v169
	v_pk_mul_f32 v[32:33], v[32:33], v[160:161]
	v_pk_mul_f32 v[28:29], v[150:151], v[28:29]
	v_pk_fma_f32 v[152:153], v[152:153], s[22:23], v[12:13] op_sel_hi:[1,0,1]
	v_pk_mul_f32 v[32:33], v[146:147], v[32:33]
	v_cvt_pk_fp8_f32 v20, v28, v29
	v_pk_fma_f32 v[148:149], v[148:149], s[22:23], v[4:5] op_sel_hi:[1,0,1]
	v_med3_f32 v152, v152, s87, v189
	v_med3_f32 v153, v153, s87, v189
	v_cvt_pk_fp8_f32 v21, v32, v33
	v_med3_f32 v148, v148, s87, v189
	v_med3_f32 v149, v149, s87, v189
	v_pk_add_f32 v[152:153], v[152:153], 1.0 op_sel_hi:[1,0]
	v_pk_mul_f32 v[30:31], v[30:31], v[158:159]
	v_pk_fma_f32 v[142:143], v[142:143], s[22:23], v[14:15] op_sel_hi:[1,0,1]
	v_pk_add_f32 v[148:149], v[148:149], 1.0 op_sel_hi:[1,0]
	v_pk_mul_f32 v[154:155], v[154:155], v[168:169]
	v_pk_mul_f32 v[28:29], v[152:153], v[30:31]
	v_pk_mul_f32 v[30:31], v[148:149], v[154:155]
	v_cvt_pk_fp8_f32 v20, v28, v29 op_sel:[0,0,1]
	v_min_f32_e32 v28, 0x40e00000, v142
	v_min_f32_e32 v29, 0x40e00000, v143
	v_cvt_pk_fp8_f32 v21, v30, v31 op_sel:[0,0,1]
	v_pk_mul_f32 v[30:31], v[28:29], s[24:25] op_sel_hi:[1,0]
	v_pk_fma_f32 v[32:33], v[138:139], s[22:23], v[10:11] op_sel_hi:[1,0,1]
	v_exp_f32_e32 v30, v30
	v_exp_f32_e32 v31, v31
	v_pk_fma_f32 v[138:139], v[144:145], s[22:23], v[16:17] op_sel_hi:[1,0,1]
	v_med3_f32 v32, v32, s87, v189
	v_min_f32_e32 v138, 0x40e00000, v138
	v_pk_add_f32 v[30:31], v[30:31], 1.0 op_sel_hi:[1,0]
	v_min_f32_e32 v139, 0x40e00000, v139
	v_rcp_f32_e32 v30, v30
	v_rcp_f32_e32 v31, v31
	v_pk_mul_f32 v[142:143], v[138:139], s[24:25] op_sel_hi:[1,0]
	v_med3_f32 v33, v33, s87, v189
	v_exp_f32_e32 v142, v142
	v_exp_f32_e32 v143, v143
	v_pk_mul_f32 v[28:29], v[28:29], v[30:31]
	v_pk_add_f32 v[30:31], v[32:33], 1.0 op_sel_hi:[1,0]
	v_pk_fma_f32 v[32:33], v[140:141], s[22:23], v[12:13] op_sel_hi:[1,0,1]
	v_pk_mul_f32 v[30:31], v[30:31], v[28:29]
	v_pk_add_f32 v[28:29], v[142:143], 1.0 op_sel_hi:[1,0]
	v_med3_f32 v32, v32, s87, v189
	v_rcp_f32_e32 v28, v28
	v_rcp_f32_e32 v29, v29
	v_med3_f32 v33, v33, s87, v189
	v_pk_add_f32 v[32:33], v[32:33], 1.0 op_sel_hi:[1,0]
	v_pk_fma_f32 v[136:137], v[136:137], s[22:23], v[8:9] op_sel_hi:[1,0,1]
	v_pk_mul_f32 v[28:29], v[138:139], v[28:29]
	v_min_f32_e32 v136, 0x40e00000, v136
	v_pk_mul_f32 v[32:33], v[32:33], v[28:29]
	v_pk_fma_f32 v[28:29], v[134:135], s[22:23], v[6:7] op_sel_hi:[1,0,1]
	v_min_f32_e32 v137, 0x40e00000, v137
	v_min_f32_e32 v28, 0x40e00000, v28
	v_min_f32_e32 v29, 0x40e00000, v29
	v_pk_mul_f32 v[134:135], v[28:29], s[24:25] op_sel_hi:[1,0]
	v_pk_mul_f32 v[138:139], v[136:137], s[24:25] op_sel_hi:[1,0]
	v_exp_f32_e32 v134, v134
	v_exp_f32_e32 v135, v135
	v_exp_f32_e32 v138, v138
	v_exp_f32_e32 v139, v139
	v_pk_fma_f32 v[130:131], v[130:131], s[22:23], v[2:3] op_sel_hi:[1,0,1]
	v_pk_add_f32 v[134:135], v[134:135], 1.0 op_sel_hi:[1,0]
	v_med3_f32 v130, v130, s87, v189
	v_rcp_f32_e32 v134, v134
	v_rcp_f32_e32 v135, v135
	v_med3_f32 v131, v131, s87, v189
	v_pk_add_f32 v[130:131], v[130:131], 1.0 op_sel_hi:[1,0]
	v_pk_fma_f32 v[132:133], v[132:133], s[22:23], v[4:5] op_sel_hi:[1,0,1]
	v_pk_mul_f32 v[28:29], v[28:29], v[134:135]
	v_med3_f32 v132, v132, s87, v189
	v_pk_mul_f32 v[130:131], v[130:131], v[28:29]
	v_pk_add_f32 v[28:29], v[138:139], 1.0 op_sel_hi:[1,0]
	v_med3_f32 v133, v133, s87, v189
	v_rcp_f32_e32 v28, v28
	v_rcp_f32_e32 v29, v29
	v_pk_fma_f32 v[122:123], v[122:123], s[22:23], v[10:11] op_sel_hi:[1,0,1]
	v_pk_fma_f32 v[118:119], v[118:119], s[22:23], v[6:7] op_sel_hi:[1,0,1]
	v_med3_f32 v122, v122, s87, v189
	v_pk_mul_f32 v[134:135], v[136:137], v[28:29]
	v_mov_b32_e32 v29, v163
	v_cvt_pk_fp8_f32 v29, v130, v131
	v_mov_b32_e32 v28, v163
	v_cvt_pk_fp8_f32 v28, v30, v31
	v_pk_add_f32 v[30:31], v[132:133], 1.0 op_sel_hi:[1,0]
	v_med3_f32 v123, v123, s87, v189
	v_pk_mul_f32 v[30:31], v[30:31], v[134:135]
	v_cvt_pk_fp8_f32 v28, v32, v33 op_sel:[0,0,1]
	v_cvt_pk_fp8_f32 v29, v30, v31 op_sel:[0,0,1]
	v_pk_fma_f32 v[30:31], v[126:127], s[22:23], v[14:15] op_sel_hi:[1,0,1]
	v_pk_fma_f32 v[126:127], v[128:129], s[22:23], v[16:17] op_sel_hi:[1,0,1]
	v_min_f32_e32 v30, 0x40e00000, v30
	v_min_f32_e32 v31, 0x40e00000, v31
	v_pk_mul_f32 v[32:33], v[30:31], s[24:25] op_sel_hi:[1,0]
	v_min_f32_e32 v126, 0x40e00000, v126
	v_exp_f32_e32 v32, v32
	v_exp_f32_e32 v33, v33
	v_min_f32_e32 v127, 0x40e00000, v127
	v_pk_mul_f32 v[128:129], v[126:127], s[24:25] op_sel_hi:[1,0]
	v_min_f32_e32 v118, 0x40e00000, v118
	v_pk_add_f32 v[32:33], v[32:33], 1.0 op_sel_hi:[1,0]
	v_exp_f32_e32 v128, v128
	v_rcp_f32_e32 v32, v32
	v_rcp_f32_e32 v33, v33
	v_exp_f32_e32 v129, v129
	v_min_f32_e32 v119, 0x40e00000, v119
	v_pk_fma_f32 v[120:121], v[120:121], s[22:23], v[8:9] op_sel_hi:[1,0,1]
	v_pk_mul_f32 v[30:31], v[30:31], v[32:33]
	v_pk_add_f32 v[32:33], v[122:123], 1.0 op_sel_hi:[1,0]
	v_pk_fma_f32 v[122:123], v[124:125], s[22:23], v[12:13] op_sel_hi:[1,0,1]
	v_pk_mul_f32 v[30:31], v[32:33], v[30:31]
	v_pk_add_f32 v[32:33], v[128:129], 1.0 op_sel_hi:[1,0]
	v_med3_f32 v122, v122, s87, v189
	v_rcp_f32_e32 v32, v32
	v_rcp_f32_e32 v33, v33
	v_med3_f32 v123, v123, s87, v189
	v_pk_add_f32 v[122:123], v[122:123], 1.0 op_sel_hi:[1,0]
	v_min_f32_e32 v120, 0x40e00000, v120
	v_pk_mul_f32 v[32:33], v[126:127], v[32:33]
	v_min_f32_e32 v121, 0x40e00000, v121
	v_pk_mul_f32 v[32:33], v[122:123], v[32:33]
	v_pk_mul_f32 v[122:123], v[118:119], s[24:25] op_sel_hi:[1,0]
	v_pk_mul_f32 v[124:125], v[120:121], s[24:25] op_sel_hi:[1,0]
	v_exp_f32_e32 v122, v122
	v_exp_f32_e32 v123, v123
	v_exp_f32_e32 v124, v124
	v_exp_f32_e32 v125, v125
	v_pk_fma_f32 v[114:115], v[114:115], s[22:23], v[2:3] op_sel_hi:[1,0,1]
	v_pk_add_f32 v[122:123], v[122:123], 1.0 op_sel_hi:[1,0]
	v_med3_f32 v114, v114, s87, v189
	v_rcp_f32_e32 v122, v122
	v_rcp_f32_e32 v123, v123
	v_med3_f32 v115, v115, s87, v189
	v_pk_add_f32 v[114:115], v[114:115], 1.0 op_sel_hi:[1,0]
	v_pk_fma_f32 v[116:117], v[116:117], s[22:23], v[4:5] op_sel_hi:[1,0,1]
	v_pk_mul_f32 v[118:119], v[118:119], v[122:123]
	v_med3_f32 v116, v116, s87, v189
	v_pk_mul_f32 v[114:115], v[114:115], v[118:119]
	v_pk_add_f32 v[118:119], v[124:125], 1.0 op_sel_hi:[1,0]
	v_med3_f32 v117, v117, s87, v189
	v_rcp_f32_e32 v118, v118
	v_rcp_f32_e32 v119, v119
	v_pk_fma_f32 v[106:107], v[106:107], s[22:23], v[10:11] op_sel_hi:[1,0,1]
	v_pk_fma_f32 v[102:103], v[102:103], s[22:23], v[6:7] op_sel_hi:[1,0,1]
	v_med3_f32 v106, v106, s87, v189
	v_pk_mul_f32 v[118:119], v[120:121], v[118:119]
	v_mov_b32_e32 v121, v163
	v_cvt_pk_fp8_f32 v121, v114, v115
	v_mov_b32_e32 v120, v163
	v_cvt_pk_fp8_f32 v120, v30, v31
	v_pk_add_f32 v[30:31], v[116:117], 1.0 op_sel_hi:[1,0]
	v_med3_f32 v107, v107, s87, v189
	v_pk_mul_f32 v[30:31], v[30:31], v[118:119]
	v_cvt_pk_fp8_f32 v120, v32, v33 op_sel:[0,0,1]
	v_cvt_pk_fp8_f32 v121, v30, v31 op_sel:[0,0,1]
	v_pk_fma_f32 v[30:31], v[110:111], s[22:23], v[14:15] op_sel_hi:[1,0,1]
	v_pk_fma_f32 v[110:111], v[112:113], s[22:23], v[16:17] op_sel_hi:[1,0,1]
	v_min_f32_e32 v30, 0x40e00000, v30
	v_min_f32_e32 v31, 0x40e00000, v31
	v_pk_mul_f32 v[32:33], v[30:31], s[24:25] op_sel_hi:[1,0]
	v_min_f32_e32 v110, 0x40e00000, v110
	v_exp_f32_e32 v32, v32
	v_exp_f32_e32 v33, v33
	v_min_f32_e32 v111, 0x40e00000, v111
	v_pk_mul_f32 v[112:113], v[110:111], s[24:25] op_sel_hi:[1,0]
	v_min_f32_e32 v102, 0x40e00000, v102
	v_pk_add_f32 v[32:33], v[32:33], 1.0 op_sel_hi:[1,0]
	v_exp_f32_e32 v112, v112
	v_rcp_f32_e32 v32, v32
	v_rcp_f32_e32 v33, v33
	v_exp_f32_e32 v113, v113
	v_min_f32_e32 v103, 0x40e00000, v103
	v_pk_fma_f32 v[104:105], v[104:105], s[22:23], v[8:9] op_sel_hi:[1,0,1]
	v_pk_mul_f32 v[30:31], v[30:31], v[32:33]
	v_pk_add_f32 v[32:33], v[106:107], 1.0 op_sel_hi:[1,0]
	v_pk_fma_f32 v[106:107], v[108:109], s[22:23], v[12:13] op_sel_hi:[1,0,1]
	v_pk_mul_f32 v[30:31], v[32:33], v[30:31]
	v_pk_add_f32 v[32:33], v[112:113], 1.0 op_sel_hi:[1,0]
	v_med3_f32 v106, v106, s87, v189
	v_rcp_f32_e32 v32, v32
	v_rcp_f32_e32 v33, v33
	v_med3_f32 v107, v107, s87, v189
	v_pk_add_f32 v[106:107], v[106:107], 1.0 op_sel_hi:[1,0]
	v_min_f32_e32 v104, 0x40e00000, v104
	v_pk_mul_f32 v[32:33], v[110:111], v[32:33]
	v_min_f32_e32 v105, 0x40e00000, v105
	v_pk_mul_f32 v[32:33], v[106:107], v[32:33]
	v_pk_mul_f32 v[106:107], v[102:103], s[24:25] op_sel_hi:[1,0]
	v_pk_mul_f32 v[108:109], v[104:105], s[24:25] op_sel_hi:[1,0]
	v_exp_f32_e32 v106, v106
	v_exp_f32_e32 v107, v107
	v_exp_f32_e32 v108, v108
	v_exp_f32_e32 v109, v109
	v_pk_fma_f32 v[98:99], v[98:99], s[22:23], v[2:3] op_sel_hi:[1,0,1]
	v_pk_add_f32 v[106:107], v[106:107], 1.0 op_sel_hi:[1,0]
	v_med3_f32 v98, v98, s87, v189
	v_rcp_f32_e32 v106, v106
	v_rcp_f32_e32 v107, v107
	v_med3_f32 v99, v99, s87, v189
	v_pk_add_f32 v[98:99], v[98:99], 1.0 op_sel_hi:[1,0]
	v_pk_fma_f32 v[100:101], v[100:101], s[22:23], v[4:5] op_sel_hi:[1,0,1]
	v_pk_mul_f32 v[102:103], v[102:103], v[106:107]
	v_med3_f32 v100, v100, s87, v189
	v_pk_mul_f32 v[98:99], v[98:99], v[102:103]
	v_pk_add_f32 v[102:103], v[108:109], 1.0 op_sel_hi:[1,0]
	v_med3_f32 v101, v101, s87, v189
	v_rcp_f32_e32 v102, v102
	v_rcp_f32_e32 v103, v103
	s_nop 0
	v_pk_mul_f32 v[102:103], v[104:105], v[102:103]
	v_mov_b32_e32 v104, v163
	v_mov_b32_e32 v105, v163
	v_cvt_pk_fp8_f32 v104, v30, v31
	v_cvt_pk_fp8_f32 v105, v98, v99
	v_pk_add_f32 v[30:31], v[100:101], 1.0 op_sel_hi:[1,0]
	v_cvt_pk_fp8_f32 v104, v32, v33 op_sel:[0,0,1]
	v_pk_mul_f32 v[30:31], v[30:31], v[102:103]
	s_nop 0
	v_cvt_pk_fp8_f32 v105, v30, v31 op_sel:[0,0,1]
	global_store_dwordx2 v[18:19], v[20:21], off
	global_store_dwordx2 v[24:25], v[28:29], off
	global_store_dwordx2 v[26:27], v[120:121], off
	global_store_dwordx2 v[22:23], v[104:105], off
	v_pk_fma_f32 v[20:21], v[94:95], s[22:23], v[14:15] op_sel_hi:[1,0,1]
	v_pk_fma_f32 v[26:27], v[96:97], s[22:23], v[16:17] op_sel_hi:[1,0,1]
	v_min_f32_e32 v20, 0x40e00000, v20
	v_min_f32_e32 v21, 0x40e00000, v21
	v_pk_mul_f32 v[22:23], v[20:21], s[24:25] op_sel_hi:[1,0]
	v_min_f32_e32 v26, 0x40e00000, v26
	v_exp_f32_e32 v22, v22
	v_exp_f32_e32 v23, v23
	v_min_f32_e32 v27, 0x40e00000, v27
	v_pk_mul_f32 v[28:29], v[26:27], s[24:25] op_sel_hi:[1,0]
	v_pk_fma_f32 v[24:25], v[90:91], s[22:23], v[10:11] op_sel_hi:[1,0,1]
	v_pk_add_f32 v[22:23], v[22:23], 1.0 op_sel_hi:[1,0]
	v_exp_f32_e32 v28, v28
	v_rcp_f32_e32 v22, v22
	v_rcp_f32_e32 v23, v23
	v_exp_f32_e32 v29, v29
	v_med3_f32 v24, v24, s87, v189
	v_med3_f32 v25, v25, s87, v189
	v_pk_mul_f32 v[20:21], v[20:21], v[22:23]
	v_pk_add_f32 v[22:23], v[24:25], 1.0 op_sel_hi:[1,0]
	v_pk_fma_f32 v[24:25], v[92:93], s[22:23], v[12:13] op_sel_hi:[1,0,1]
	v_pk_mul_f32 v[20:21], v[22:23], v[20:21]
	v_pk_add_f32 v[22:23], v[28:29], 1.0 op_sel_hi:[1,0]
	v_med3_f32 v24, v24, s87, v189
	v_rcp_f32_e32 v22, v22
	v_rcp_f32_e32 v23, v23
	v_med3_f32 v25, v25, s87, v189
	v_pk_add_f32 v[24:25], v[24:25], 1.0 op_sel_hi:[1,0]
	v_pk_fma_f32 v[30:31], v[88:89], s[22:23], v[8:9] op_sel_hi:[1,0,1]
	v_pk_mul_f32 v[22:23], v[26:27], v[22:23]
	v_min_f32_e32 v30, 0x40e00000, v30
	v_pk_mul_f32 v[22:23], v[24:25], v[22:23]
	v_pk_fma_f32 v[24:25], v[86:87], s[22:23], v[6:7] op_sel_hi:[1,0,1]
	v_min_f32_e32 v31, 0x40e00000, v31
	v_min_f32_e32 v24, 0x40e00000, v24
	v_min_f32_e32 v25, 0x40e00000, v25
	v_pk_mul_f32 v[26:27], v[24:25], s[24:25] op_sel_hi:[1,0]
	v_pk_mul_f32 v[32:33], v[30:31], s[24:25] op_sel_hi:[1,0]
	v_exp_f32_e32 v26, v26
	v_exp_f32_e32 v27, v27
	v_exp_f32_e32 v32, v32
	v_exp_f32_e32 v33, v33
	v_pk_fma_f32 v[28:29], v[82:83], s[22:23], v[2:3] op_sel_hi:[1,0,1]
	v_pk_add_f32 v[26:27], v[26:27], 1.0 op_sel_hi:[1,0]
	v_med3_f32 v28, v28, s87, v189
	v_rcp_f32_e32 v26, v26
	v_rcp_f32_e32 v27, v27
	v_med3_f32 v29, v29, s87, v189
	v_pk_mul_f32 v[24:25], v[24:25], v[26:27]
	v_pk_add_f32 v[26:27], v[28:29], 1.0 op_sel_hi:[1,0]
	v_pk_fma_f32 v[28:29], v[84:85], s[22:23], v[4:5] op_sel_hi:[1,0,1]
	v_pk_mul_f32 v[24:25], v[26:27], v[24:25]
	v_pk_add_f32 v[26:27], v[32:33], 1.0 op_sel_hi:[1,0]
	v_med3_f32 v28, v28, s87, v189
	v_rcp_f32_e32 v26, v26
	v_rcp_f32_e32 v27, v27
	v_med3_f32 v29, v29, s87, v189
	v_pk_mul_f32 v[26:27], v[30:31], v[26:27]
	v_mov_b32_e32 v30, v163
	v_mov_b32_e32 v31, v163
	v_cvt_pk_fp8_f32 v30, v20, v21
	v_cvt_pk_fp8_f32 v31, v24, v25
	v_pk_add_f32 v[20:21], v[28:29], 1.0 op_sel_hi:[1,0]
	v_pk_fma_f32 v[24:25], v[74:75], s[22:23], v[10:11] op_sel_hi:[1,0,1]
	v_pk_mul_f32 v[20:21], v[20:21], v[26:27]
	v_cvt_pk_fp8_f32 v30, v22, v23 op_sel:[0,0,1]
	v_cvt_pk_fp8_f32 v31, v20, v21 op_sel:[0,0,1]
	v_add_co_u32_e32 v20, vcc, s6, v18
	v_pk_fma_f32 v[26:27], v[80:81], s[22:23], v[16:17] op_sel_hi:[1,0,1]
	s_nop 0
	v_addc_co_u32_e32 v21, vcc, 0, v19, vcc
	global_store_dwordx2 v[20:21], v[30:31], off
	v_pk_fma_f32 v[20:21], v[78:79], s[22:23], v[14:15] op_sel_hi:[1,0,1]
	v_min_f32_e32 v26, 0x40e00000, v26
	v_min_f32_e32 v20, 0x40e00000, v20
	v_min_f32_e32 v21, 0x40e00000, v21
	v_pk_mul_f32 v[22:23], v[20:21], s[24:25] op_sel_hi:[1,0]
	v_min_f32_e32 v27, 0x40e00000, v27
	v_exp_f32_e32 v22, v22
	v_exp_f32_e32 v23, v23
	v_pk_mul_f32 v[28:29], v[26:27], s[24:25] op_sel_hi:[1,0]
	v_med3_f32 v24, v24, s87, v189
	v_exp_f32_e32 v28, v28
	v_pk_add_f32 v[22:23], v[22:23], 1.0 op_sel_hi:[1,0]
	v_exp_f32_e32 v29, v29
	v_rcp_f32_e32 v22, v22
	v_rcp_f32_e32 v23, v23
	v_med3_f32 v25, v25, s87, v189
	v_pk_fma_f32 v[30:31], v[72:73], s[22:23], v[8:9] op_sel_hi:[1,0,1]
	s_mov_b32 s6, 0x48000
	v_pk_mul_f32 v[20:21], v[20:21], v[22:23]
	v_pk_add_f32 v[22:23], v[24:25], 1.0 op_sel_hi:[1,0]
	v_pk_fma_f32 v[24:25], v[76:77], s[22:23], v[12:13] op_sel_hi:[1,0,1]
	v_pk_mul_f32 v[20:21], v[22:23], v[20:21]
	v_pk_add_f32 v[22:23], v[28:29], 1.0 op_sel_hi:[1,0]
	v_med3_f32 v24, v24, s87, v189
	v_rcp_f32_e32 v22, v22
	v_rcp_f32_e32 v23, v23
	v_med3_f32 v25, v25, s87, v189
	v_pk_add_f32 v[24:25], v[24:25], 1.0 op_sel_hi:[1,0]
	v_min_f32_e32 v30, 0x40e00000, v30
	v_pk_mul_f32 v[22:23], v[26:27], v[22:23]
	v_min_f32_e32 v31, 0x40e00000, v31
	v_pk_mul_f32 v[22:23], v[24:25], v[22:23]
	v_pk_fma_f32 v[24:25], v[70:71], s[22:23], v[6:7] op_sel_hi:[1,0,1]
	v_pk_mul_f32 v[32:33], v[30:31], s[24:25] op_sel_hi:[1,0]
	v_min_f32_e32 v24, 0x40e00000, v24
	v_min_f32_e32 v25, 0x40e00000, v25
	v_pk_mul_f32 v[26:27], v[24:25], s[24:25] op_sel_hi:[1,0]
	v_exp_f32_e32 v32, v32
	v_exp_f32_e32 v26, v26
	v_exp_f32_e32 v27, v27
	v_exp_f32_e32 v33, v33
	v_pk_fma_f32 v[28:29], v[66:67], s[22:23], v[2:3] op_sel_hi:[1,0,1]
	v_pk_add_f32 v[26:27], v[26:27], 1.0 op_sel_hi:[1,0]
	s_nop 0
	v_rcp_f32_e32 v26, v26
	v_rcp_f32_e32 v27, v27
	v_med3_f32 v28, v28, s87, v189
	v_med3_f32 v29, v29, s87, v189
	v_pk_mul_f32 v[24:25], v[24:25], v[26:27]
	v_pk_add_f32 v[26:27], v[28:29], 1.0 op_sel_hi:[1,0]
	v_pk_fma_f32 v[28:29], v[68:69], s[22:23], v[4:5] op_sel_hi:[1,0,1]
	v_pk_mul_f32 v[24:25], v[26:27], v[24:25]
	v_pk_add_f32 v[26:27], v[32:33], 1.0 op_sel_hi:[1,0]
	v_med3_f32 v28, v28, s87, v189
	v_rcp_f32_e32 v26, v26
	v_rcp_f32_e32 v27, v27
	v_med3_f32 v29, v29, s87, v189
	v_pk_mul_f32 v[26:27], v[30:31], v[26:27]
	v_mov_b32_e32 v30, v163
	v_mov_b32_e32 v31, v163
	v_cvt_pk_fp8_f32 v30, v20, v21
	v_cvt_pk_fp8_f32 v31, v24, v25
	v_pk_add_f32 v[20:21], v[28:29], 1.0 op_sel_hi:[1,0]
	v_pk_fma_f32 v[24:25], v[58:59], s[22:23], v[10:11] op_sel_hi:[1,0,1]
	v_pk_mul_f32 v[20:21], v[20:21], v[26:27]
	v_cvt_pk_fp8_f32 v30, v22, v23 op_sel:[0,0,1]
	v_cvt_pk_fp8_f32 v31, v20, v21 op_sel:[0,0,1]
	v_add_co_u32_e32 v20, vcc, s6, v18
	v_pk_fma_f32 v[26:27], v[64:65], s[22:23], v[16:17] op_sel_hi:[1,0,1]
	s_nop 0
	v_addc_co_u32_e32 v21, vcc, 0, v19, vcc
	global_store_dwordx2 v[20:21], v[30:31], off
	v_pk_fma_f32 v[20:21], v[62:63], s[22:23], v[14:15] op_sel_hi:[1,0,1]
	v_min_f32_e32 v26, 0x40e00000, v26
	v_min_f32_e32 v20, 0x40e00000, v20
	v_min_f32_e32 v21, 0x40e00000, v21
	v_pk_mul_f32 v[22:23], v[20:21], s[24:25] op_sel_hi:[1,0]
	v_min_f32_e32 v27, 0x40e00000, v27
	v_exp_f32_e32 v22, v22
	v_exp_f32_e32 v23, v23
	v_pk_mul_f32 v[28:29], v[26:27], s[24:25] op_sel_hi:[1,0]
	v_med3_f32 v24, v24, s87, v189
	v_exp_f32_e32 v28, v28
	v_pk_add_f32 v[22:23], v[22:23], 1.0 op_sel_hi:[1,0]
	v_exp_f32_e32 v29, v29
	v_rcp_f32_e32 v22, v22
	v_rcp_f32_e32 v23, v23
	v_med3_f32 v25, v25, s87, v189
	v_pk_fma_f32 v[30:31], v[56:57], s[22:23], v[8:9] op_sel_hi:[1,0,1]
	s_mov_b32 s6, 0x50000
	v_pk_mul_f32 v[20:21], v[20:21], v[22:23]
	v_pk_add_f32 v[22:23], v[24:25], 1.0 op_sel_hi:[1,0]
	v_pk_fma_f32 v[24:25], v[60:61], s[22:23], v[12:13] op_sel_hi:[1,0,1]
	v_pk_mul_f32 v[20:21], v[22:23], v[20:21]
	v_pk_add_f32 v[22:23], v[28:29], 1.0 op_sel_hi:[1,0]
	v_med3_f32 v24, v24, s87, v189
	v_rcp_f32_e32 v22, v22
	v_rcp_f32_e32 v23, v23
	v_med3_f32 v25, v25, s87, v189
	v_pk_add_f32 v[24:25], v[24:25], 1.0 op_sel_hi:[1,0]
	v_min_f32_e32 v30, 0x40e00000, v30
	v_pk_mul_f32 v[22:23], v[26:27], v[22:23]
	v_min_f32_e32 v31, 0x40e00000, v31
	v_pk_mul_f32 v[22:23], v[24:25], v[22:23]
	v_pk_fma_f32 v[24:25], v[54:55], s[22:23], v[6:7] op_sel_hi:[1,0,1]
	v_pk_mul_f32 v[32:33], v[30:31], s[24:25] op_sel_hi:[1,0]
	v_min_f32_e32 v24, 0x40e00000, v24
	v_min_f32_e32 v25, 0x40e00000, v25
	v_pk_mul_f32 v[26:27], v[24:25], s[24:25] op_sel_hi:[1,0]
	v_exp_f32_e32 v32, v32
	v_exp_f32_e32 v26, v26
	v_exp_f32_e32 v27, v27
	v_exp_f32_e32 v33, v33
	v_pk_fma_f32 v[28:29], v[50:51], s[22:23], v[2:3] op_sel_hi:[1,0,1]
	v_pk_fma_f32 v[14:15], v[46:47], s[22:23], v[14:15] op_sel_hi:[1,0,1]
	v_pk_add_f32 v[26:27], v[26:27], 1.0 op_sel_hi:[1,0]
	v_med3_f32 v28, v28, s87, v189
	v_rcp_f32_e32 v26, v26
	v_rcp_f32_e32 v27, v27
	v_med3_f32 v29, v29, s87, v189
	v_min_f32_e32 v14, 0x40e00000, v14
	v_min_f32_e32 v15, 0x40e00000, v15
	v_pk_mul_f32 v[24:25], v[24:25], v[26:27]
	v_pk_add_f32 v[26:27], v[28:29], 1.0 op_sel_hi:[1,0]
	v_pk_fma_f32 v[28:29], v[52:53], s[22:23], v[4:5] op_sel_hi:[1,0,1]
	v_pk_mul_f32 v[24:25], v[26:27], v[24:25]
	v_pk_add_f32 v[26:27], v[32:33], 1.0 op_sel_hi:[1,0]
	v_med3_f32 v28, v28, s87, v189
	v_rcp_f32_e32 v26, v26
	v_rcp_f32_e32 v27, v27
	v_med3_f32 v29, v29, s87, v189
	v_pk_fma_f32 v[16:17], v[48:49], s[22:23], v[16:17] op_sel_hi:[1,0,1]
	v_pk_fma_f32 v[10:11], v[42:43], s[22:23], v[10:11] op_sel_hi:[1,0,1]
	v_pk_mul_f32 v[26:27], v[30:31], v[26:27]
	v_mov_b32_e32 v30, v163
	v_mov_b32_e32 v31, v163
	v_cvt_pk_fp8_f32 v30, v20, v21
	v_cvt_pk_fp8_f32 v31, v24, v25
	v_pk_add_f32 v[20:21], v[28:29], 1.0 op_sel_hi:[1,0]
	v_min_f32_e32 v16, 0x40e00000, v16
	v_pk_mul_f32 v[20:21], v[20:21], v[26:27]
	v_cvt_pk_fp8_f32 v30, v22, v23 op_sel:[0,0,1]
	v_cvt_pk_fp8_f32 v31, v20, v21 op_sel:[0,0,1]
	v_add_co_u32_e32 v20, vcc, s6, v18
	v_min_f32_e32 v17, 0x40e00000, v17
	s_nop 0
	v_addc_co_u32_e32 v21, vcc, 0, v19, vcc
	global_store_dwordx2 v[20:21], v[30:31], off
	v_pk_mul_f32 v[20:21], v[14:15], s[24:25] op_sel_hi:[1,0]
	v_pk_mul_f32 v[22:23], v[16:17], s[24:25] op_sel_hi:[1,0]
	v_exp_f32_e32 v20, v20
	v_exp_f32_e32 v21, v21
	v_exp_f32_e32 v22, v22
	v_exp_f32_e32 v23, v23
	v_med3_f32 v10, v10, s87, v189
	v_pk_add_f32 v[20:21], v[20:21], 1.0 op_sel_hi:[1,0]
	v_med3_f32 v11, v11, s87, v189
	v_rcp_f32_e32 v20, v20
	v_rcp_f32_e32 v21, v21
	v_pk_add_f32 v[10:11], v[10:11], 1.0 op_sel_hi:[1,0]
	v_pk_fma_f32 v[12:13], v[44:45], s[22:23], v[12:13] op_sel_hi:[1,0,1]
	v_pk_fma_f32 v[6:7], v[38:39], s[22:23], v[6:7] op_sel_hi:[1,0,1]
	v_pk_mul_f32 v[14:15], v[14:15], v[20:21]
	v_med3_f32 v12, v12, s87, v189
	v_pk_mul_f32 v[10:11], v[10:11], v[14:15]
	v_pk_add_f32 v[14:15], v[22:23], 1.0 op_sel_hi:[1,0]
	v_med3_f32 v13, v13, s87, v189
	v_rcp_f32_e32 v14, v14
	v_rcp_f32_e32 v15, v15
	v_pk_add_f32 v[12:13], v[12:13], 1.0 op_sel_hi:[1,0]
	v_min_f32_e32 v6, 0x40e00000, v6
	v_min_f32_e32 v7, 0x40e00000, v7
	v_pk_mul_f32 v[14:15], v[16:17], v[14:15]
	v_pk_fma_f32 v[8:9], v[40:41], s[22:23], v[8:9] op_sel_hi:[1,0,1]
	v_pk_mul_f32 v[12:13], v[12:13], v[14:15]
	v_pk_mul_f32 v[14:15], v[6:7], s[24:25] op_sel_hi:[1,0]
	v_min_f32_e32 v8, 0x40e00000, v8
	v_exp_f32_e32 v14, v14
	v_exp_f32_e32 v15, v15
	v_min_f32_e32 v9, 0x40e00000, v9
	v_pk_mul_f32 v[16:17], v[8:9], s[24:25] op_sel_hi:[1,0]
	v_pk_fma_f32 v[2:3], v[34:35], s[22:23], v[2:3] op_sel_hi:[1,0,1]
	v_pk_add_f32 v[14:15], v[14:15], 1.0 op_sel_hi:[1,0]
	v_exp_f32_e32 v16, v16
	v_rcp_f32_e32 v14, v14
	v_rcp_f32_e32 v15, v15
	v_exp_f32_e32 v17, v17
	v_med3_f32 v2, v2, s87, v189
	v_med3_f32 v3, v3, s87, v189
	v_pk_mul_f32 v[6:7], v[6:7], v[14:15]
	v_pk_add_f32 v[2:3], v[2:3], 1.0 op_sel_hi:[1,0]
	v_pk_fma_f32 v[4:5], v[36:37], s[22:23], v[4:5] op_sel_hi:[1,0,1]
	v_pk_mul_f32 v[2:3], v[2:3], v[6:7]
	v_pk_add_f32 v[6:7], v[16:17], 1.0 op_sel_hi:[1,0]
	v_med3_f32 v4, v4, s87, v189
	v_rcp_f32_e32 v6, v6
	v_rcp_f32_e32 v7, v7
	v_med3_f32 v5, v5, s87, v189
	v_pk_mul_f32 v[6:7], v[8:9], v[6:7]
	v_mov_b32_e32 v8, v163
	v_mov_b32_e32 v9, v163
	v_cvt_pk_fp8_f32 v8, v10, v11
	v_cvt_pk_fp8_f32 v9, v2, v3
	v_pk_add_f32 v[2:3], v[4:5], 1.0 op_sel_hi:[1,0]
	v_cvt_pk_fp8_f32 v8, v12, v13 op_sel:[0,0,1]
	v_pk_mul_f32 v[2:3], v[2:3], v[6:7]
	s_nop 0
	v_cvt_pk_fp8_f32 v9, v2, v3 op_sel:[0,0,1]
	v_add_co_u32_e32 v2, vcc, 0x58000, v18
	s_nop 1
	v_addc_co_u32_e32 v3, vcc, 0, v19, vcc
	s_andn2_b64 vcc, exec, s[4:5]
	s_mov_b64 s[4:5], -1
	global_store_dwordx2 v[2:3], v[8:9], off
	s_cbranch_vccnz .LBB0_1348
	s_andn2_b64 vcc, exec, s[12:13]
	s_cbranch_vccnz .LBB0_1347
	s_barrier
	s_branch .LBB0_1347

.LBB0_1443:
	s_ashr_i32 s41, s40, 31
	s_lshl_b64 s[40:41], s[40:41], 13
	v_lshl_or_b32 v20, s10, 8, v183
	s_add_u32 s40, s12, s40
	s_addc_u32 s41, s13, s41
	v_ashrrev_i32_e32 v21, 31, v20
	v_lshl_add_u64 v[2:3], v[20:21], 2, s[40:41]
	global_load_dwordx4 v[14:17], v[2:3], off
	global_load_dwordx4 v[10:13], v[2:3], off offset:16
	global_load_dwordx4 v[6:9], v[2:3], off offset:512
	s_nop 0
	global_load_dwordx4 v[2:5], v[2:3], off offset:528
	v_mov_b32_e32 v24, 0
	v_mov_b32_e32 v25, 0
	v_mov_b32_e32 v26, 0
	v_mov_b32_e32 v27, 0
	v_mov_b32_e32 v28, 0
	v_mov_b32_e32 v29, 0
	v_mov_b32_e32 v30, 0
	v_mov_b32_e32 v31, 0
	v_lshl_add_u32 v18, s85, 8, v1
	v_mov_b32_e32 v174, 0
	v_mov_b32_e32 v175, 0
	v_ashrrev_i32_e32 v19, 31, v18
	v_or_b32_e32 v22, 16, v18
	v_or_b32_e32 v176, 32, v18
	v_or_b32_e32 v178, 48, v18
	v_lshlrev_b64 v[18:19], 11, v[18:19]
	v_ashrrev_i32_e32 v23, 31, v22
	v_lshl_add_u64 v[18:19], s[18:19], 0, v[18:19]
	v_lshlrev_b64 v[22:23], 11, v[22:23]
	v_lshl_add_u64 v[18:19], v[18:19], 0, v[20:21]
	v_lshl_add_u64 v[22:23], s[18:19], 0, v[22:23]
	v_lshl_add_u64 v[180:181], v[22:23], 0, v[20:21]
	v_mov_b32_e32 v32, 0
	v_mov_b32_e32 v33, 0
	v_ashrrev_i32_e32 v177, 31, v176
	v_ashrrev_i32_e32 v179, 31, v178
	v_lshlrev_b64 v[176:177], 11, v[176:177]
	v_lshlrev_b64 v[178:179], 11, v[178:179]
	v_lshl_add_u64 v[176:177], s[18:19], 0, v[176:177]
	v_lshl_add_u64 v[178:179], s[18:19], 0, v[178:179]
	v_lshl_add_u64 v[176:177], v[176:177], 0, v[20:21]
	v_lshl_add_u64 v[178:179], v[178:179], 0, v[20:21]
	v_lshl_add_u64 v[188:189], v[18:19], 0, s[14:15]
	v_lshl_add_u64 v[190:191], v[18:19], 0, s[24:25]
	v_lshl_add_u64 v[22:23], v[18:19], 0, s[26:27]
	v_lshl_add_u64 v[20:21], v[18:19], 0, s[28:29]
	s_waitcnt vmcnt(0)
	v_pk_fma_f32 v[158:159], v[158:159], s[30:31], v[14:15] op_sel_hi:[1,0,1]
	v_pk_fma_f32 v[154:155], v[154:155], s[30:31], v[10:11] op_sel_hi:[1,0,1]
	v_pk_fma_f32 v[138:139], v[138:139], s[30:31], v[6:7] op_sel_hi:[1,0,1]
	v_pk_fma_f32 v[130:131], v[130:131], s[30:31], v[2:3] op_sel_hi:[1,0,1]
	v_cvt_pk_fp8_f32 v24, v158, v159
	v_cvt_pk_fp8_f32 v25, v154, v155
	v_pk_fma_f32 v[150:151], v[150:151], s[30:31], v[14:15] op_sel_hi:[1,0,1]
	v_pk_fma_f32 v[146:147], v[146:147], s[30:31], v[10:11] op_sel_hi:[1,0,1]
	v_cvt_pk_fp8_f32 v26, v138, v139
	v_cvt_pk_fp8_f32 v27, v130, v131
	v_pk_fma_f32 v[126:127], v[126:127], s[30:31], v[6:7] op_sel_hi:[1,0,1]
	v_pk_fma_f32 v[122:123], v[122:123], s[30:31], v[2:3] op_sel_hi:[1,0,1]
	v_cvt_pk_fp8_f32 v28, v150, v151
	v_cvt_pk_fp8_f32 v29, v146, v147
	v_pk_fma_f32 v[160:161], v[160:161], s[30:31], v[16:17] op_sel_hi:[1,0,1]
	v_pk_fma_f32 v[156:157], v[156:157], s[30:31], v[12:13] op_sel_hi:[1,0,1]
	v_cvt_pk_fp8_f32 v30, v126, v127
	v_cvt_pk_fp8_f32 v31, v122, v123
	v_pk_fma_f32 v[140:141], v[140:141], s[30:31], v[8:9] op_sel_hi:[1,0,1]
	v_pk_fma_f32 v[132:133], v[132:133], s[30:31], v[4:5] op_sel_hi:[1,0,1]
	v_pk_fma_f32 v[114:115], v[114:115], s[30:31], v[6:7] op_sel_hi:[1,0,1]
	v_pk_fma_f32 v[106:107], v[106:107], s[30:31], v[2:3] op_sel_hi:[1,0,1]
	v_cvt_pk_fp8_f32 v24, v160, v161 op_sel:[0,0,1]
	v_cvt_pk_fp8_f32 v25, v156, v157 op_sel:[0,0,1]
	v_pk_fma_f32 v[152:153], v[152:153], s[30:31], v[16:17] op_sel_hi:[1,0,1]
	v_pk_fma_f32 v[148:149], v[148:149], s[30:31], v[12:13] op_sel_hi:[1,0,1]
	v_cvt_pk_fp8_f32 v174, v114, v115
	v_cvt_pk_fp8_f32 v26, v140, v141 op_sel:[0,0,1]
	v_cvt_pk_fp8_f32 v27, v132, v133 op_sel:[0,0,1]
	v_cvt_pk_fp8_f32 v175, v106, v107
	v_pk_fma_f32 v[128:129], v[128:129], s[30:31], v[8:9] op_sel_hi:[1,0,1]
	v_pk_fma_f32 v[124:125], v[124:125], s[30:31], v[4:5] op_sel_hi:[1,0,1]
	v_cvt_pk_fp8_f32 v28, v152, v153 op_sel:[0,0,1]
	v_cvt_pk_fp8_f32 v29, v148, v149 op_sel:[0,0,1]
	v_cvt_pk_fp8_f32 v30, v128, v129 op_sel:[0,0,1]
	v_cvt_pk_fp8_f32 v31, v124, v125 op_sel:[0,0,1]
	global_store_dwordx2 v[18:19], v[24:25], off
	global_store_dwordx2 v[18:19], v[26:27], off offset:128
	global_store_dwordx2 v[180:181], v[28:29], off
	global_store_dwordx2 v[180:181], v[30:31], off offset:128
	v_pk_fma_f32 v[24:25], v[116:117], s[30:31], v[8:9] op_sel_hi:[1,0,1]
	v_pk_fma_f32 v[26:27], v[108:109], s[30:31], v[4:5] op_sel_hi:[1,0,1]
	v_cvt_pk_fp8_f32 v174, v24, v25 op_sel:[0,0,1]
	v_cvt_pk_fp8_f32 v175, v26, v27 op_sel:[0,0,1]
	v_pk_fma_f32 v[24:25], v[118:119], s[30:31], v[14:15] op_sel_hi:[1,0,1]
	v_pk_fma_f32 v[26:27], v[110:111], s[30:31], v[10:11] op_sel_hi:[1,0,1]
	v_mov_b32_e32 v28, 0
	v_mov_b32_e32 v29, 0
	v_cvt_pk_fp8_f32 v28, v24, v25
	v_cvt_pk_fp8_f32 v29, v26, v27
	v_pk_fma_f32 v[142:143], v[142:143], s[30:31], v[14:15] op_sel_hi:[1,0,1]
	v_pk_fma_f32 v[134:135], v[134:135], s[30:31], v[10:11] op_sel_hi:[1,0,1]
	v_cvt_pk_fp8_f32 v32, v142, v143
	v_cvt_pk_fp8_f32 v33, v134, v135
	v_pk_fma_f32 v[24:25], v[120:121], s[30:31], v[16:17] op_sel_hi:[1,0,1]
	v_pk_fma_f32 v[26:27], v[112:113], s[30:31], v[12:13] op_sel_hi:[1,0,1]
	v_cvt_pk_fp8_f32 v28, v24, v25 op_sel:[0,0,1]
	v_cvt_pk_fp8_f32 v29, v26, v27 op_sel:[0,0,1]
	v_pk_fma_f32 v[24:25], v[102:103], s[30:31], v[6:7] op_sel_hi:[1,0,1]
	v_pk_fma_f32 v[26:27], v[98:99], s[30:31], v[2:3] op_sel_hi:[1,0,1]
	v_mov_b32_e32 v30, 0
	v_mov_b32_e32 v31, 0
	v_pk_fma_f32 v[144:145], v[144:145], s[30:31], v[16:17] op_sel_hi:[1,0,1]
	v_pk_fma_f32 v[136:137], v[136:137], s[30:31], v[12:13] op_sel_hi:[1,0,1]
	v_cvt_pk_fp8_f32 v30, v24, v25
	v_cvt_pk_fp8_f32 v31, v26, v27
	v_cvt_pk_fp8_f32 v32, v144, v145 op_sel:[0,0,1]
	v_cvt_pk_fp8_f32 v33, v136, v137 op_sel:[0,0,1]
	v_pk_fma_f32 v[24:25], v[104:105], s[30:31], v[8:9] op_sel_hi:[1,0,1]
	v_pk_fma_f32 v[26:27], v[100:101], s[30:31], v[4:5] op_sel_hi:[1,0,1]
	v_cvt_pk_fp8_f32 v30, v24, v25 op_sel:[0,0,1]
	v_cvt_pk_fp8_f32 v31, v26, v27 op_sel:[0,0,1]
	global_store_dwordx2 v[176:177], v[32:33], off
	global_store_dwordx2 v[176:177], v[174:175], off offset:128
	global_store_dwordx2 v[178:179], v[28:29], off
	global_store_dwordx2 v[178:179], v[30:31], off offset:128
	v_pk_fma_f32 v[24:25], v[94:95], s[30:31], v[14:15] op_sel_hi:[1,0,1]
	v_pk_fma_f32 v[26:27], v[90:91], s[30:31], v[10:11] op_sel_hi:[1,0,1]
	v_mov_b32_e32 v28, 0
	v_mov_b32_e32 v29, 0
	v_cvt_pk_fp8_f32 v28, v24, v25
	v_cvt_pk_fp8_f32 v29, v26, v27
	v_pk_fma_f32 v[24:25], v[96:97], s[30:31], v[16:17] op_sel_hi:[1,0,1]
	v_pk_fma_f32 v[26:27], v[92:93], s[30:31], v[12:13] op_sel_hi:[1,0,1]
	v_cvt_pk_fp8_f32 v28, v24, v25 op_sel:[0,0,1]
	v_cvt_pk_fp8_f32 v29, v26, v27 op_sel:[0,0,1]
	v_pk_fma_f32 v[24:25], v[82:83], s[30:31], v[6:7] op_sel_hi:[1,0,1]
	v_pk_fma_f32 v[26:27], v[70:71], s[30:31], v[2:3] op_sel_hi:[1,0,1]
	v_mov_b32_e32 v30, 0
	v_mov_b32_e32 v31, 0
	v_cvt_pk_fp8_f32 v30, v24, v25
	v_cvt_pk_fp8_f32 v31, v26, v27
	v_pk_fma_f32 v[24:25], v[84:85], s[30:31], v[8:9] op_sel_hi:[1,0,1]
	v_pk_fma_f32 v[26:27], v[72:73], s[30:31], v[4:5] op_sel_hi:[1,0,1]
	v_cvt_pk_fp8_f32 v30, v24, v25 op_sel:[0,0,1]
	v_cvt_pk_fp8_f32 v31, v26, v27 op_sel:[0,0,1]
	v_add_co_u32_e32 v24, vcc, s58, v18
	v_pk_fma_f32 v[26:27], v[66:67], s[30:31], v[10:11] op_sel_hi:[1,0,1]
	s_nop 0
	v_addc_co_u32_e32 v25, vcc, 0, v19, vcc
	global_store_dwordx2 v[24:25], v[28:29], off
	global_store_dwordx2 v[188:189], v[30:31], off offset:128
	v_pk_fma_f32 v[24:25], v[78:79], s[30:31], v[14:15] op_sel_hi:[1,0,1]
	v_mov_b32_e32 v28, 0
	v_mov_b32_e32 v29, 0
	v_cvt_pk_fp8_f32 v28, v24, v25
	v_cvt_pk_fp8_f32 v29, v26, v27
	v_pk_fma_f32 v[24:25], v[80:81], s[30:31], v[16:17] op_sel_hi:[1,0,1]
	v_pk_fma_f32 v[26:27], v[68:69], s[30:31], v[12:13] op_sel_hi:[1,0,1]
	v_cvt_pk_fp8_f32 v28, v24, v25 op_sel:[0,0,1]
	v_cvt_pk_fp8_f32 v29, v26, v27 op_sel:[0,0,1]
	v_pk_fma_f32 v[24:25], v[54:55], s[30:31], v[6:7] op_sel_hi:[1,0,1]
	v_pk_fma_f32 v[26:27], v[42:43], s[30:31], v[2:3] op_sel_hi:[1,0,1]
	v_mov_b32_e32 v30, 0
	v_mov_b32_e32 v31, 0
	v_cvt_pk_fp8_f32 v30, v24, v25
	v_cvt_pk_fp8_f32 v31, v26, v27
	v_pk_fma_f32 v[24:25], v[56:57], s[30:31], v[8:9] op_sel_hi:[1,0,1]
	v_pk_fma_f32 v[26:27], v[44:45], s[30:31], v[4:5] op_sel_hi:[1,0,1]
	v_cvt_pk_fp8_f32 v30, v24, v25 op_sel:[0,0,1]
	v_cvt_pk_fp8_f32 v31, v26, v27 op_sel:[0,0,1]
	v_add_co_u32_e32 v24, vcc, s82, v18
	v_pk_fma_f32 v[26:27], v[46:47], s[30:31], v[10:11] op_sel_hi:[1,0,1]
	s_nop 0
	v_addc_co_u32_e32 v25, vcc, 0, v19, vcc
	global_store_dwordx2 v[24:25], v[28:29], off
	global_store_dwordx2 v[190:191], v[30:31], off offset:128
	v_pk_fma_f32 v[24:25], v[50:51], s[30:31], v[14:15] op_sel_hi:[1,0,1]
	v_mov_b32_e32 v28, 0
	v_mov_b32_e32 v29, 0
	v_cvt_pk_fp8_f32 v28, v24, v25
	v_cvt_pk_fp8_f32 v29, v26, v27
	v_pk_fma_f32 v[24:25], v[52:53], s[30:31], v[16:17] op_sel_hi:[1,0,1]
	v_pk_fma_f32 v[26:27], v[48:49], s[30:31], v[12:13] op_sel_hi:[1,0,1]
	v_cvt_pk_fp8_f32 v28, v24, v25 op_sel:[0,0,1]
	v_cvt_pk_fp8_f32 v29, v26, v27 op_sel:[0,0,1]
	v_pk_fma_f32 v[24:25], v[74:75], s[30:31], v[6:7] op_sel_hi:[1,0,1]
	v_pk_fma_f32 v[26:27], v[86:87], s[30:31], v[2:3] op_sel_hi:[1,0,1]
	v_mov_b32_e32 v30, 0
	v_mov_b32_e32 v31, 0
	v_cvt_pk_fp8_f32 v30, v24, v25
	v_cvt_pk_fp8_f32 v31, v26, v27
	v_pk_fma_f32 v[24:25], v[76:77], s[30:31], v[8:9] op_sel_hi:[1,0,1]
	v_pk_fma_f32 v[26:27], v[88:89], s[30:31], v[4:5] op_sel_hi:[1,0,1]
	v_cvt_pk_fp8_f32 v30, v24, v25 op_sel:[0,0,1]
	v_cvt_pk_fp8_f32 v31, v26, v27 op_sel:[0,0,1]
	v_add_co_u32_e32 v24, vcc, s83, v18
	v_pk_fma_f32 v[14:15], v[38:39], s[30:31], v[14:15] op_sel_hi:[1,0,1]
	s_nop 0
	v_addc_co_u32_e32 v25, vcc, 0, v19, vcc
	global_store_dwordx2 v[24:25], v[28:29], off
	global_store_dwordx2 v[22:23], v[30:31], off offset:128
	v_mov_b32_e32 v22, 0
	v_cvt_pk_fp8_f32 v22, v14, v15
	v_pk_fma_f32 v[10:11], v[34:35], s[30:31], v[10:11] op_sel_hi:[1,0,1]
	v_mov_b32_e32 v23, 0
	v_cvt_pk_fp8_f32 v23, v10, v11
	v_pk_fma_f32 v[10:11], v[40:41], s[30:31], v[16:17] op_sel_hi:[1,0,1]
	v_pk_fma_f32 v[6:7], v[58:59], s[30:31], v[6:7] op_sel_hi:[1,0,1]
	v_cvt_pk_fp8_f32 v22, v10, v11 op_sel:[0,0,1]
	v_pk_fma_f32 v[2:3], v[62:63], s[30:31], v[2:3] op_sel_hi:[1,0,1]
	v_mov_b32_e32 v10, 0
	v_mov_b32_e32 v11, 0
	v_cvt_pk_fp8_f32 v10, v6, v7
	v_cvt_pk_fp8_f32 v11, v2, v3
	v_pk_fma_f32 v[12:13], v[36:37], s[30:31], v[12:13] op_sel_hi:[1,0,1]
	v_pk_fma_f32 v[2:3], v[60:61], s[30:31], v[8:9] op_sel_hi:[1,0,1]
	v_cvt_pk_fp8_f32 v23, v12, v13 op_sel:[0,0,1]
	v_pk_fma_f32 v[4:5], v[64:65], s[30:31], v[4:5] op_sel_hi:[1,0,1]
	v_cvt_pk_fp8_f32 v10, v2, v3 op_sel:[0,0,1]
	v_cvt_pk_fp8_f32 v11, v4, v5 op_sel:[0,0,1]
	v_add_co_u32_e32 v2, vcc, s84, v18
	s_nop 1
	v_addc_co_u32_e32 v3, vcc, 0, v19, vcc
	s_andn2_b64 vcc, exec, s[6:7]
	s_mov_b64 s[6:7], -1
	global_store_dwordx2 v[2:3], v[22:23], off
	global_store_dwordx2 v[20:21], v[10:11], off offset:128
	s_cbranch_vccnz .LBB0_1434
	s_andn2_b64 vcc, exec, s[16:17]
	s_cbranch_vccnz .LBB0_1433
	s_barrier
	s_branch .LBB0_1433
